# baseline (speedup 1.0000x reference)
.Lattn_map:
	v_readfirstlane_b32 s101, v104
	s_nop 0
	v_mov_b32_e32 v84, s101
	s_cmp_ge_i32 s101, s68
	s_cbranch_scc1 .LBB0_95
	s_lshl_b32 s94, s101, 2
	s_add_i32 s94, s94, 0x26dd0
	v_mov_b32_e32 v2, s94
	ds_read_b32 v84, v2
	s_sub_i32 s94, s68, 16
	s_cmp_lt_i32 s101, s94
	s_cbranch_scc1 .LBB0_95
	s_setprio 2
	s_sub_i32 s94, s68, 6
	s_cmp_lt_i32 s101, s94
	s_cbranch_scc1 .LBB0_95
	s_setprio 3
	s_branch .LBB0_95
